# prep32 stage A: the next pass's two row loads are prefetched one pass ahead into spare registers (second in-pass wait removed)
# baseline (speedup 1.0000x reference)
.LBB0_240:
	s_mov_b32 s5, 0
	s_mov_b64 s[2:3], -1
	s_movk_i32 s6, 0x1c00
	v_add_u32_e32 v56, s76, v186
	v_mad_i64_i32 v[56:57], s[2:3], v56, s6, v[150:151]
	global_load_dwordx4 v[246:249], v[56:57], off
	global_load_dwordx2 v[172:173], v[56:57], off offset:512
	global_load_dwordx2 v[210:211], v[56:57], off offset:520
	s_mov_b64 s[2:3], -1
	s_mov_b32 s8, 0x3f07dc22
	s_mov_b32 s10, 0x3f35f0e3
	s_mov_b32 s12, 0xbe11a98e
	s_mov_b32 s14, 0x3e027906
.LBB0_241:
	v_cndmask_b32_e64 v0, 0, 1, s[2:3]
	v_cmp_ne_u32_e64 s[0:1], 1, v0
	v_add_u32_e32 v0, s5, v186
	s_waitcnt vmcnt(0)
	v_add_u32_e32 v50, s76, v0
	v_add_u32_e32 v56, 16, v50
	v_mad_i64_i32 v[56:57], s[2:3], v56, s6, v[150:151]
	v_mov_b64_e32 v[46:47], v[246:247]
	v_mov_b64_e32 v[48:49], v[248:249]
	v_mov_b64_e32 v[52:53], v[172:173]
	v_mov_b64_e32 v[54:55], v[210:211]
	global_load_dwordx4 v[246:249], v[56:57], off
	global_load_dwordx2 v[172:173], v[56:57], off offset:512
	global_load_dwordx2 v[210:211], v[56:57], off offset:520
	s_mov_b32 s2, 0xbf3a00e3
	v_mov_b64_e32 v[58:59], s[2:3]
	v_ashrrev_i32_e32 v51, 31, v50
	v_lshlrev_b64 v[50:51], 9, v[50:51]
	v_lshl_add_u64 v[50:51], v[110:111], 0, v[50:51]
	s_mov_b32 s5, 16
	v_lshlrev_b32_e32 v56, 16, v52
	v_and_b32_e32 v62, 0xffff0000, v52
	v_fma_f32 v52, |v56|, s49, 1.0
	v_rcp_f32_e32 v52, v52
	v_lshlrev_b32_e32 v63, 16, v53
	v_and_b32_e32 v64, 0xffff0000, v53
	v_cmp_gt_f32_e32 vcc, 0, v56
	v_fmamk_f32 v53, v52, 0x3f07dc22, v205
	v_fmaak_f32 v53, v52, v53, 0x3f35f0e3
	v_fmaak_f32 v53, v52, v53, 0xbe11a98e
	v_fmaak_f32 v53, v52, v53, 0x3e027906
	v_mul_f32_e32 v52, v52, v53
	v_mul_f32_e32 v53, -0.5, v56
	v_mul_f32_e32 v53, v53, v56
	v_mul_f32_e32 v53, 0x3fb8aa3b, v53
	v_exp_f32_e32 v53, v53
	v_lshlrev_b32_e32 v65, 16, v54
	v_and_b32_e32 v66, 0xffff0000, v54
	v_lshlrev_b32_e32 v67, 16, v55
	v_mul_f32_e32 v52, v53, v52
	v_mul_f32_e32 v53, v52, v56
	v_fma_f32 v52, -v52, v56, v56
	v_cndmask_b32_e32 v69, v52, v53, vcc
	v_lshlrev_b32_e32 v52, 16, v46
	v_and_b32_e32 v53, 0xffff0000, v46
	v_fma_f32 v46, |v52|, s49, 1.0
	v_rcp_f32_e32 v54, v46
	v_mul_f32_e32 v46, -0.5, v52
	v_mul_f32_e32 v46, v46, v52
	v_mul_f32_e32 v46, 0x3fb8aa3b, v46
	v_exp_f32_e32 v56, v46
	v_fma_f32 v46, |v53|, s49, 1.0
	v_and_b32_e32 v68, 0xffff0000, v55
	v_rcp_f32_e32 v55, v46
	v_mul_f32_e32 v46, -0.5, v53
	v_mul_f32_e32 v46, v46, v53
	v_mul_f32_e32 v46, 0x3fb8aa3b, v46
	v_pk_fma_f32 v[60:61], v[54:55], s[8:9], v[58:59] op_sel_hi:[1,0,0]
	v_exp_f32_e32 v57, v46
	v_pk_fma_f32 v[60:61], v[54:55], v[60:61], s[10:11] op_sel_hi:[1,1,0]
	v_fma_f32 v46, |v62|, s49, 1.0
	v_pk_fma_f32 v[60:61], v[54:55], v[60:61], s[12:13] op_sel_hi:[1,1,0]
	v_rcp_f32_e32 v46, v46
	v_pk_fma_f32 v[60:61], v[54:55], v[60:61], s[14:15] op_sel_hi:[1,1,0]
	v_cmp_gt_f32_e32 vcc, 0, v52
	v_pk_mul_f32 v[54:55], v[54:55], v[60:61]
	v_cmp_gt_f32_e64 s[2:3], 0, v53
	v_pk_mul_f32 v[54:55], v[56:57], v[54:55]
	v_add_f32_e32 v70, 0, v69
	v_pk_mul_f32 v[56:57], v[54:55], v[52:53]
	v_pk_fma_f32 v[52:53], v[54:55], v[52:53], v[52:53] neg_lo:[1,0,0] neg_hi:[1,0,0]
	s_nop 0
	v_cndmask_b32_e32 v61, v52, v56, vcc
	v_fmamk_f32 v52, v46, 0x3f07dc22, v205
	v_fmaak_f32 v52, v46, v52, 0x3f35f0e3
	v_fmaak_f32 v52, v46, v52, 0xbe11a98e
	v_fmaak_f32 v52, v46, v52, 0x3e027906
	v_mul_f32_e32 v46, v46, v52
	v_mul_f32_e32 v52, -0.5, v62
	v_mul_f32_e32 v52, v52, v62
	v_mul_f32_e32 v52, 0x3fb8aa3b, v52
	v_exp_f32_e32 v52, v52
	v_cmp_gt_f32_e32 vcc, 0, v62
	v_cndmask_b32_e64 v60, v53, v57, s[2:3]
	v_mul_f32_e32 v46, v52, v46
	v_mul_f32_e32 v52, v46, v62
	v_fma_f32 v46, -v46, v62, v62
	v_cndmask_b32_e32 v62, v46, v52, vcc
	v_fma_f32 v52, |v63|, s49, 1.0
	v_rcp_f32_e32 v52, v52
	v_cmp_gt_f32_e32 vcc, 0, v63
	v_add_f32_e32 v46, v62, v70
	v_fmamk_f32 v53, v52, 0x3f07dc22, v205
	v_fmaak_f32 v53, v52, v53, 0x3f35f0e3
	v_fmaak_f32 v53, v52, v53, 0xbe11a98e
	v_fmaak_f32 v53, v52, v53, 0x3e027906
	v_mul_f32_e32 v52, v52, v53
	v_mul_f32_e32 v53, -0.5, v63
	v_mul_f32_e32 v53, v53, v63
	v_mul_f32_e32 v53, 0x3fb8aa3b, v53
	v_exp_f32_e32 v53, v53
	s_nop 0
	v_mul_f32_e32 v52, v53, v52
	v_mul_f32_e32 v53, v52, v63
	v_fma_f32 v52, -v52, v63, v63
	v_cndmask_b32_e32 v63, v52, v53, vcc
	v_add_f32_e32 v70, v63, v46
	v_lshlrev_b32_e32 v46, 16, v47
	v_mul_f32_e32 v53, -0.5, v46
	v_mul_f32_e32 v53, v53, v46
	v_and_b32_e32 v47, 0xffff0000, v47
	v_mul_f32_e32 v53, 0x3fb8aa3b, v53
	v_fma_f32 v52, |v46|, s49, 1.0
	v_exp_f32_e32 v54, v53
	v_fma_f32 v53, |v47|, s49, 1.0
	v_rcp_f32_e32 v52, v52
	v_rcp_f32_e32 v53, v53
	v_mul_f32_e32 v55, -0.5, v47
	v_mul_f32_e32 v55, v55, v47
	v_mul_f32_e32 v55, 0x3fb8aa3b, v55
	v_pk_fma_f32 v[56:57], v[52:53], s[8:9], v[58:59] op_sel_hi:[1,0,0]
	v_exp_f32_e32 v55, v55
	v_pk_fma_f32 v[56:57], v[52:53], v[56:57], s[10:11] op_sel_hi:[1,1,0]
	v_cmp_gt_f32_e32 vcc, 0, v46
	v_pk_fma_f32 v[56:57], v[52:53], v[56:57], s[12:13] op_sel_hi:[1,1,0]
	v_cmp_gt_f32_e64 s[2:3], 0, v47
	v_pk_fma_f32 v[56:57], v[52:53], v[56:57], s[14:15] op_sel_hi:[1,1,0]
	s_nop 0
	v_pk_mul_f32 v[52:53], v[52:53], v[56:57]
	s_nop 0
	v_pk_mul_f32 v[52:53], v[54:55], v[52:53]
	s_nop 0
	v_pk_mul_f32 v[54:55], v[52:53], v[46:47]
	v_pk_fma_f32 v[46:47], v[52:53], v[46:47], v[46:47] neg_lo:[1,0,0] neg_hi:[1,0,0]
	s_nop 0
	v_cndmask_b32_e32 v72, v46, v54, vcc
	v_fma_f32 v46, |v64|, s49, 1.0
	v_rcp_f32_e32 v46, v46
	v_cndmask_b32_e64 v71, v47, v55, s[2:3]
	v_cmp_gt_f32_e32 vcc, 0, v64
	v_fmamk_f32 v47, v46, 0x3f07dc22, v205
	v_fmaak_f32 v47, v46, v47, 0x3f35f0e3
	v_fmaak_f32 v47, v46, v47, 0xbe11a98e
	v_fmaak_f32 v47, v46, v47, 0x3e027906
	v_mul_f32_e32 v46, v46, v47
	v_mul_f32_e32 v47, -0.5, v64
	v_mul_f32_e32 v47, v47, v64
	v_mul_f32_e32 v47, 0x3fb8aa3b, v47
	v_exp_f32_e32 v47, v47
	s_nop 0
	v_mul_f32_e32 v46, v47, v46
	v_mul_f32_e32 v47, v46, v64
	v_fma_f32 v46, -v46, v64, v64
	v_cndmask_b32_e32 v64, v46, v47, vcc
	v_fma_f32 v47, |v65|, s49, 1.0
	v_rcp_f32_e32 v47, v47
	v_cmp_gt_f32_e32 vcc, 0, v65
	v_add_f32_e32 v46, v64, v70
	v_fmamk_f32 v52, v47, 0x3f07dc22, v205
	v_fmaak_f32 v52, v47, v52, 0x3f35f0e3
	v_fmaak_f32 v52, v47, v52, 0xbe11a98e
	v_fmaak_f32 v52, v47, v52, 0x3e027906
	v_mul_f32_e32 v47, v47, v52
	v_mul_f32_e32 v52, -0.5, v65
	v_mul_f32_e32 v52, v52, v65
	v_mul_f32_e32 v52, 0x3fb8aa3b, v52
	v_exp_f32_e32 v52, v52
	s_nop 0
	v_mul_f32_e32 v47, v52, v47
	v_mul_f32_e32 v52, v47, v65
	v_fma_f32 v47, -v47, v65, v65
	v_cndmask_b32_e32 v65, v47, v52, vcc
	v_add_f32_e32 v70, v65, v46
	v_lshlrev_b32_e32 v46, 16, v48
	v_and_b32_e32 v47, 0xffff0000, v48
	v_fma_f32 v48, |v46|, s49, 1.0
	v_rcp_f32_e32 v52, v48
	v_mul_f32_e32 v48, -0.5, v46
	v_mul_f32_e32 v48, v48, v46
	v_mul_f32_e32 v48, 0x3fb8aa3b, v48
	v_exp_f32_e32 v54, v48
	v_fma_f32 v48, |v47|, s49, 1.0
	v_rcp_f32_e32 v53, v48
	v_mul_f32_e32 v48, -0.5, v47
	v_mul_f32_e32 v48, v48, v47
	v_mul_f32_e32 v48, 0x3fb8aa3b, v48
	v_pk_fma_f32 v[56:57], v[52:53], s[8:9], v[58:59] op_sel_hi:[1,0,0]
	v_exp_f32_e32 v55, v48
	v_pk_fma_f32 v[56:57], v[52:53], v[56:57], s[10:11] op_sel_hi:[1,1,0]
	v_cmp_gt_f32_e32 vcc, 0, v46
	v_pk_fma_f32 v[56:57], v[52:53], v[56:57], s[12:13] op_sel_hi:[1,1,0]
	v_cmp_gt_f32_e64 s[2:3], 0, v47
	v_pk_fma_f32 v[56:57], v[52:53], v[56:57], s[14:15] op_sel_hi:[1,1,0]
	s_nop 0
	v_pk_mul_f32 v[52:53], v[52:53], v[56:57]
	s_nop 0
	v_pk_mul_f32 v[52:53], v[54:55], v[52:53]
	s_nop 0
	v_pk_mul_f32 v[54:55], v[52:53], v[46:47]
	v_pk_fma_f32 v[46:47], v[52:53], v[46:47], v[46:47] neg_lo:[1,0,0] neg_hi:[1,0,0]
	s_nop 0
	v_cndmask_b32_e32 v57, v46, v54, vcc
	v_fma_f32 v46, |v66|, s49, 1.0
	v_rcp_f32_e32 v46, v46
	v_cndmask_b32_e64 v56, v47, v55, s[2:3]
	v_cmp_gt_f32_e32 vcc, 0, v66
	v_fmamk_f32 v47, v46, 0x3f07dc22, v205
	v_fmaak_f32 v47, v46, v47, 0x3f35f0e3
	v_fmaak_f32 v47, v46, v47, 0xbe11a98e
	v_fmaak_f32 v47, v46, v47, 0x3e027906
	v_mul_f32_e32 v46, v46, v47
	v_mul_f32_e32 v47, -0.5, v66
	v_mul_f32_e32 v47, v47, v66
	v_mul_f32_e32 v47, 0x3fb8aa3b, v47
	v_exp_f32_e32 v47, v47
	s_nop 0
	v_mul_f32_e32 v46, v47, v46
	v_mul_f32_e32 v47, v46, v66
	v_fma_f32 v46, -v46, v66, v66
	v_cndmask_b32_e32 v66, v46, v47, vcc
	v_fma_f32 v47, |v67|, s49, 1.0
	v_rcp_f32_e32 v47, v47
	v_cmp_gt_f32_e32 vcc, 0, v67
	v_add_f32_e32 v46, v66, v70
	v_fmamk_f32 v48, v47, 0x3f07dc22, v205
	v_fmaak_f32 v48, v47, v48, 0x3f35f0e3
	v_fmaak_f32 v48, v47, v48, 0xbe11a98e
	v_fmaak_f32 v48, v47, v48, 0x3e027906
	v_mul_f32_e32 v47, v47, v48
	v_mul_f32_e32 v48, -0.5, v67
	v_mul_f32_e32 v48, v48, v67
	v_mul_f32_e32 v48, 0x3fb8aa3b, v48
	v_exp_f32_e32 v48, v48
	s_nop 0
	v_mul_f32_e32 v47, v48, v47
	v_mul_f32_e32 v48, v47, v67
	v_fma_f32 v47, -v47, v67, v67
	v_cndmask_b32_e32 v67, v47, v48, vcc
	v_add_f32_e32 v70, v67, v46
	v_lshlrev_b32_e32 v46, 16, v49
	v_and_b32_e32 v47, 0xffff0000, v49
	v_mul_f32_e32 v49, -0.5, v46
	v_mul_f32_e32 v49, v49, v46
	v_mul_f32_e32 v49, 0x3fb8aa3b, v49
	v_fma_f32 v48, |v46|, s49, 1.0
	v_exp_f32_e32 v52, v49
	v_fma_f32 v49, |v47|, s49, 1.0
	v_rcp_f32_e32 v48, v48
	v_rcp_f32_e32 v49, v49
	v_mul_f32_e32 v53, -0.5, v47
	v_mul_f32_e32 v53, v53, v47
	v_mul_f32_e32 v53, 0x3fb8aa3b, v53
	v_pk_fma_f32 v[54:55], v[48:49], s[8:9], v[58:59] op_sel_hi:[1,0,0]
	v_exp_f32_e32 v53, v53
	v_pk_fma_f32 v[54:55], v[48:49], v[54:55], s[10:11] op_sel_hi:[1,1,0]
	v_cmp_gt_f32_e32 vcc, 0, v46
	v_pk_fma_f32 v[54:55], v[48:49], v[54:55], s[12:13] op_sel_hi:[1,1,0]
	v_cmp_gt_f32_e64 s[2:3], 0, v47
	v_pk_fma_f32 v[54:55], v[48:49], v[54:55], s[14:15] op_sel_hi:[1,1,0]
	s_nop 0
	v_pk_mul_f32 v[48:49], v[48:49], v[54:55]
	s_nop 0
	v_pk_mul_f32 v[48:49], v[52:53], v[48:49]
	s_nop 0
	v_pk_mul_f32 v[52:53], v[48:49], v[46:47]
	v_pk_fma_f32 v[46:47], v[48:49], v[46:47], v[46:47] neg_lo:[1,0,0] neg_hi:[1,0,0]
	v_cvt_pk_bf16_f32 v48, v57, v56
	v_cndmask_b32_e32 v52, v46, v52, vcc
	v_fma_f32 v46, |v68|, s49, 1.0
	v_rcp_f32_e32 v46, v46
	v_cndmask_b32_e64 v49, v47, v53, s[2:3]
	v_cmp_gt_f32_e32 vcc, 0, v68
	v_cvt_pk_bf16_f32 v49, v52, v49
	v_fmamk_f32 v47, v46, 0x3f07dc22, v205
	v_fmaak_f32 v47, v46, v47, 0x3f35f0e3
	v_fmaak_f32 v47, v46, v47, 0xbe11a98e
	v_fmaak_f32 v47, v46, v47, 0x3e027906
	v_mul_f32_e32 v46, v46, v47
	v_mul_f32_e32 v47, -0.5, v68
	v_mul_f32_e32 v47, v47, v68
	v_mul_f32_e32 v47, 0x3fb8aa3b, v47
	v_exp_f32_e32 v47, v47
	s_nop 0
	v_mul_f32_e32 v46, v47, v46
	v_mul_f32_e32 v47, v46, v68
	v_fma_f32 v46, -v46, v68, v68
	v_cndmask_b32_e32 v68, v46, v47, vcc
	v_add_f32_e32 v53, v68, v70
	v_cvt_pk_bf16_f32 v46, v61, v60
	v_cvt_pk_bf16_f32 v47, v72, v71
	global_store_dwordx4 v[50:51], v[46:49], off
	ds_bpermute_b32 v46, v191, v53
	s_waitcnt lgkmcnt(0)
	v_add_f32_e32 v46, v53, v46
	ds_bpermute_b32 v47, v193, v46
	s_waitcnt lgkmcnt(0)
	v_add_f32_e32 v46, v46, v47
	ds_bpermute_b32 v47, v194, v46
	s_waitcnt lgkmcnt(0)
	v_add_f32_e32 v46, v46, v47
	ds_bpermute_b32 v47, v195, v46
	s_waitcnt lgkmcnt(0)
	v_add_f32_e32 v46, v46, v47
	ds_bpermute_b32 v47, v196, v46
	s_waitcnt lgkmcnt(0)
	v_add_f32_e32 v46, v46, v47
	v_fmac_f32_e32 v62, 0xbb800000, v46
	v_fmac_f32_e32 v69, 0xbb800000, v46
	v_mul_f32_e32 v47, v62, v62
	v_fmac_f32_e32 v47, v69, v69
	v_fmac_f32_e32 v63, 0xbb800000, v46
	v_fmac_f32_e32 v47, v63, v63
	v_fmac_f32_e32 v64, 0xbb800000, v46
	v_fmac_f32_e32 v47, v64, v64
	v_fmac_f32_e32 v65, 0xbb800000, v46
	v_fmac_f32_e32 v47, v65, v65
	v_fmac_f32_e32 v66, 0xbb800000, v46
	v_fmac_f32_e32 v47, v66, v66
	v_fmac_f32_e32 v67, 0xbb800000, v46
	v_fmac_f32_e32 v47, v67, v67
	v_fmac_f32_e32 v68, 0xbb800000, v46
	v_fmac_f32_e32 v47, v68, v68
	ds_bpermute_b32 v46, v191, v47
	s_waitcnt lgkmcnt(0)
	v_add_f32_e32 v46, v47, v46
	ds_bpermute_b32 v47, v193, v46
	s_waitcnt lgkmcnt(0)
	v_add_f32_e32 v46, v46, v47
	ds_bpermute_b32 v47, v194, v46
	s_waitcnt lgkmcnt(0)
	v_add_f32_e32 v46, v46, v47
	ds_bpermute_b32 v47, v195, v46
	s_waitcnt lgkmcnt(0)
	v_add_f32_e32 v46, v46, v47
	ds_bpermute_b32 v47, v196, v46
	s_waitcnt lgkmcnt(0)
	v_add_f32_e32 v46, v46, v47
	v_fmamk_f32 v46, v46, 0x3b800000, v206
	v_cmp_gt_f32_e32 vcc, s45, v46
	v_mul_f32_e32 v47, 0x4f800000, v46
	s_nop 0
	v_cndmask_b32_e32 v46, v46, v47, vcc
	v_sqrt_f32_e32 v47, v46
	s_nop 0
	v_add_u32_e32 v48, -1, v47
	v_fma_f32 v49, -v48, v47, v46
	v_cmp_ge_f32_e64 s[2:3], 0, v49
	v_add_u32_e32 v49, 1, v47
	s_nop 0
	v_cndmask_b32_e64 v48, v47, v48, s[2:3]
	v_fma_f32 v47, -v49, v47, v46
	v_cmp_lt_f32_e64 s[2:3], 0, v47
	s_nop 1
	v_cndmask_b32_e64 v47, v48, v49, s[2:3]
	v_mul_f32_e32 v48, 0x37800000, v47
	v_cndmask_b32_e32 v47, v47, v48, vcc
	v_cmp_class_f32_e32 vcc, v46, v207
	s_nop 1
	v_cndmask_b32_e32 v46, v47, v46, vcc
	v_div_scale_f32 v47, s[2:3], v46, v46, 1.0
	v_rcp_f32_e32 v48, v47
	s_mov_b64 s[2:3], 0
	v_fma_f32 v49, -v47, v48, 1.0
	v_fmac_f32_e32 v48, v49, v48
	v_div_scale_f32 v49, vcc, 1.0, v46, 1.0
	v_mul_f32_e32 v50, v49, v48
	v_fma_f32 v51, -v47, v50, v49
	v_fmac_f32_e32 v50, v51, v48
	v_fma_f32 v47, -v47, v50, v49
	v_div_fmas_f32 v47, v47, v48, v50
	v_div_fixup_f32 v70, v47, v46, 1.0
	global_load_dwordx4 v[46:49], v[116:117], off offset:16
	global_load_dwordx4 v[50:53], v[116:117], off
	global_load_dwordx4 v[54:57], v[118:119], off offset:16
	global_load_dwordx4 v[58:61], v[118:119], off
	v_mul_f32_e32 v69, v69, v70
	s_and_b64 vcc, exec, s[0:1]
	s_waitcnt vmcnt(0)
	v_fma_f32 v50, v50, v69, v58
	v_bitop3_b32 v69, v0, 24, v187 bitop3:0x48
	v_lshlrev_b32_e32 v69, 1, v69
	v_cvt_pk_bf16_f32 v50, v50, s0
	v_add_u32_e32 v71, v197, v69
	ds_write_b16 v71, v50
	v_mul_f32_e32 v50, v62, v70
	v_fma_f32 v50, v51, v50, v59
	v_xor_b32_e32 v58, v0, v187
	v_cvt_pk_bf16_f32 v50, v50, s0
	v_add_u32_e32 v51, v198, v69
	ds_write_b16 v51, v50
	v_mul_f32_e32 v50, v63, v70
	v_bitop3_b32 v51, v58, 8, 24 bitop3:0x6c
	v_fma_f32 v50, v52, v50, v60
	v_lshlrev_b32_e32 v51, 1, v51
	v_cvt_pk_bf16_f32 v50, v50, s0
	v_add_u32_e32 v52, v199, v51
	ds_write_b16 v52, v50
	v_mul_f32_e32 v50, v64, v70
	v_fmac_f32_e32 v61, v53, v50
	v_cvt_pk_bf16_f32 v50, v61, s0
	v_add_u32_e32 v51, v200, v51
	ds_write_b16 v51, v50
	v_mul_f32_e32 v50, v65, v70
	v_fma_f32 v46, v46, v50, v54
	v_bitop3_b32 v50, v58, 16, 24 bitop3:0x6c
	v_lshlrev_b32_e32 v50, 1, v50
	v_cvt_pk_bf16_f32 v46, v46, s0
	v_add_u32_e32 v51, v201, v50
	ds_write_b16 v51, v46
	v_mul_f32_e32 v46, v66, v70
	v_fma_f32 v46, v47, v46, v55
	v_cvt_pk_bf16_f32 v46, v46, s0
	v_add_u32_e32 v47, v202, v50
	ds_write_b16 v47, v46
	v_mul_f32_e32 v46, v67, v70
	v_bitop3_b32 v0, v0, 24, v187 bitop3:0x84
	v_fma_f32 v46, v48, v46, v56
	v_lshlrev_b32_e32 v0, 1, v0
	v_cvt_pk_bf16_f32 v46, v46, s0
	v_add_u32_e32 v47, v203, v0
	ds_write_b16 v47, v46
	v_mul_f32_e32 v46, v68, v70
	v_fmac_f32_e32 v57, v49, v46
	v_cvt_pk_bf16_f32 v46, v57, s0
	v_add_u32_e32 v0, v223, v0
	ds_write_b16 v0, v46
	s_cbranch_vccz .LBB0_241
	s_ashr_i32 s0, s74, 31
	s_lshr_b32 s0, s0, 25
	s_add_i32 s0, s74, s0
	s_ashr_i32 s88, s0, 7
	s_ashr_i32 s89, s88, 31
	s_lshl_b64 s[0:1], s[88:89], 21
	v_readlane_b32 s2, v254, 0
	s_add_u32 s0, s2, s0
	v_readlane_b32 s2, v254, 2
	s_addc_u32 s1, s2, s1
	s_ashr_i32 s5, s4, 31
	s_waitcnt lgkmcnt(0)
	s_barrier
	s_lshl_b64 s[86:87], s[4:5], 1
	ds_read_b128 v[46:49], v231
	s_add_u32 s0, s0, s86
	s_addc_u32 s1, s1, s87
	v_mov_b32_e32 v153, v1
	v_lshl_add_u64 v[50:51], s[0:1], 0, v[152:153]
	v_lshl_add_u64 v[52:53], v[50:51], 0, v[120:121]
	s_waitcnt lgkmcnt(0)
	global_store_dwordx4 v[52:53], v[46:49], off
	ds_read_b128 v[46:49], v232
	v_lshl_add_u64 v[50:51], v[50:51], 0, v[122:123]
	v_mov_b32_e32 v0, v175
	v_readlane_b32 s0, v252, 35
	s_movk_i32 s44, 0x1c00
	s_waitcnt lgkmcnt(0)
	global_store_dwordx4 v[50:51], v[46:49], off
	s_mov_b32 s4, 0
	v_and_b32_e32 v50, 0xff, v0
	v_mov_b32_e32 v47, 0x1200
	v_lshl_add_u32 v48, v50, 2, v47
	global_load_dword v47, v48, s[64:65]
	s_nop 0
	global_load_dword v48, v48, s[66:67]
	v_lshlrev_b32_e32 v49, 1, v50
	v_add_u32_e32 v46, 0, v49
	v_cmp_lt_u32_e32 vcc, 63, v50
	v_add_u32_e32 v49, s0, v49
	v_cmp_gt_u32_e64 s[0:1], s92, v50
	s_branch .LBB0_244
